# two scanner waves share each row (half each, own raw list), so 500 rows are streamed concurrently instead of 1000; gatherer fast path merges the two lists
# speedup vs baseline: 1.0142x; 1.0132x over previous
_Z11attn_kernelPKfS0_PKDv8_DF16_S0_Pfi:
	s_load_dwordx2 s[28:29], s[0:1], 0x0
	v_cmp_gt_u32_e32 vcc, 8, v0
	s_and_saveexec_b64 s[4:5], vcc
	v_lshlrev_b32_e32 v1, 2, v0
	v_mov_b32_e32 v2, 0
	ds_write_b32 v1, v2 offset:36864
	s_or_b64 exec, exec, s[4:5]
	s_load_dword s33, s[0:1], 0x28
	v_bfe_u32 v1, v0, 6, 2
	v_lshl_or_b32 v82, s2, 2, v1
	v_readfirstlane_b32 s34, v0
	s_cmp_gt_u32 s34, 0xff
	s_cbranch_scc1 .Lsc_early_skip
	v_and_b32_e32 v3, 63, v0
	v_lshlrev_b32_e32 v2, 4, v3
	s_lshr_b32 s35, s34, 6
	s_and_b32 s55, s35, 1
	s_lshr_b32 s41, s35, 1
	s_mul_i32 s43, s55, 0x5000
	s_lshl_b32 s37, s2, 1
	s_add_u32 s37, s37, s41
	s_and_b32 s47, s37, 1
	s_lshl_b32 s47, s47, 2
	s_mul_i32 s38, s37, 0x9c40
	s_lshl_b32 s40, s47, 4
	s_sub_u32 s38, s38, s40
	s_add_u32 s38, s38, s43
	s_waitcnt lgkmcnt(0)
	s_and_b32 s29, s29, 0xffff
	s_mov_b32 s30, 0x17d78400
	s_mov_b32 s31, 0x20000
	v_max_u32_e32 v12, s47, v3
	v_lshlrev_b32_e32 v12, 4, v12
	s_cmp_eq_u32 s55, 0
	s_cbranch_scc1 .Lsc_pf1
	v_mov_b32_e32 v12, v2
.Lsc_pf1:
	buffer_load_dwordx4 v[100:103], v12, s[28:31], s38 offen nt
	s_add_u32 s40, s38, 0x400
	buffer_load_dwordx4 v[104:107], v2, s[28:31], s40 offen nt
	s_add_u32 s40, s38, 0x800
	buffer_load_dwordx4 v[108:111], v2, s[28:31], s40 offen nt
	s_add_u32 s40, s38, 0xc00
	buffer_load_dwordx4 v[112:115], v2, s[28:31], s40 offen nt
	s_add_u32 s40, s38, 0x1000
	buffer_load_dwordx4 v[116:119], v2, s[28:31], s40 offen nt
	s_add_u32 s40, s38, 0x1400
	buffer_load_dwordx4 v[120:123], v2, s[28:31], s40 offen nt
	s_add_u32 s40, s38, 0x1800
	buffer_load_dwordx4 v[124:127], v2, s[28:31], s40 offen nt
	s_add_u32 s40, s38, 0x1c00
	buffer_load_dwordx4 v[128:131], v2, s[28:31], s40 offen nt
	s_add_u32 s40, s38, 0x2000
	buffer_load_dwordx4 v[132:135], v2, s[28:31], s40 offen nt
	s_add_u32 s40, s38, 0x2400
	buffer_load_dwordx4 v[136:139], v2, s[28:31], s40 offen nt
.Lsc_early_skip:
	s_waitcnt lgkmcnt(0)
	s_barrier
	v_cmp_gt_i32_e32 vcc, s33, v82
	s_and_saveexec_b64 s[4:5], vcc
	s_cbranch_execz .LBB1_384
	s_abs_i32 s3, s33
	v_cvt_f32_u32_e32 v2, s3
	s_movk_i32 s4, 0xff
	v_sub_u32_e32 v3, 0x270f, v82
	v_cmp_lt_u32_e32 vcc, s4, v0
	v_rcp_iflag_f32_e32 v2, v2
	v_sub_u32_e32 v5, 0, v3
	s_sub_i32 s4, 0, s3
	v_xor_b32_e32 v4, s33, v3
	v_mul_f32_e32 v2, 0x4f7ffffe, v2
	v_cvt_u32_f32_e32 v2, v2
	v_max_i32_e32 v3, v3, v5
	v_ashrrev_i32_e32 v4, 31, v4
	v_mul_lo_u32 v5, s4, v2
	v_mul_hi_u32 v5, v2, v5
	v_add_u32_e32 v2, v2, v5
	v_mul_hi_u32 v2, v3, v2
	v_mul_lo_u32 v5, v2, s3
	v_sub_u32_e32 v3, v3, v5
	v_add_u32_e32 v5, 1, v2
	v_cmp_le_u32_e64 s[4:5], s3, v3
	v_and_b32_e32 v83, 63, v0
	s_nop 0
	v_cndmask_b32_e64 v2, v2, v5, s[4:5]
	v_subrev_u32_e32 v5, s3, v3
	v_cndmask_b32_e64 v3, v3, v5, s[4:5]
	v_add_u32_e32 v5, 1, v2
	v_cmp_le_u32_e64 s[4:5], s3, v3
	s_nop 1
	v_cndmask_b32_e64 v2, v2, v5, s[4:5]
	v_xor_b32_e32 v2, v2, v4
	v_sub_u32_e32 v84, v2, v4
	s_and_saveexec_b64 s[4:5], vcc
	s_xor_b64 s[30:31], exec, s[4:5]
	s_cbranch_execz .LBB1_217
	v_cmp_lt_i32_e32 vcc, -1, v84
	s_and_saveexec_b64 s[34:35], vcc
	s_cbranch_execz .LBB1_216
	s_load_dwordx8 s[20:27], s[0:1], 0x8
	v_and_b32_e32 v69, 15, v0
	v_mov_b32_e32 v0, 0x8000
	v_lshrrev_b32_e32 v67, 4, v83
	v_lshl_or_b32 v88, v1, 10, v0
	s_mul_i32 s3, s2, 0x2710
	v_mul_u32_u24_e32 v0, 0x9c4, v1
	v_lshl_or_b32 v89, v69, 2, v67
	v_add3_u32 v90, s3, v0, v83
	v_lshlrev_b32_e32 v0, 2, v1
	v_mov_b32_e32 v2, 0x9000
	v_lshl_or_b32 v91, s2, 4, v0
	v_lshlrev_b32_e32 v0, 3, v89
	v_mov_b32_e32 v32, 0
	v_lshl_or_b32 v65, v1, 3, v2
	v_or_b32_e32 v2, 0x1e00, v0
	v_mov_b32_e32 v3, v32
	s_waitcnt lgkmcnt(0)
	v_lshl_add_u64 v[34:35], s[20:21], 0, v[2:3]
	v_or_b32_e32 v2, 0x1c00, v0
	v_lshl_add_u64 v[36:37], s[20:21], 0, v[2:3]
	v_or_b32_e32 v2, 0x1a00, v0
	v_lshl_add_u64 v[38:39], s[20:21], 0, v[2:3]
	v_or_b32_e32 v2, 0x1800, v0
	v_lshl_add_u64 v[40:41], s[20:21], 0, v[2:3]
	v_or_b32_e32 v2, 0x1600, v0
	v_lshl_add_u64 v[42:43], s[20:21], 0, v[2:3]
	v_or_b32_e32 v2, 0x1400, v0
	v_lshlrev_b32_e32 v63, 12, v1
	v_lshl_add_u64 v[44:45], s[20:21], 0, v[2:3]
	v_or_b32_e32 v2, 0x1200, v0
	v_mov_b32_e32 v1, v32
	v_lshl_or_b32 v71, v83, 3, v63
	v_lshl_or_b32 v73, v67, 3, v63
	v_lshl_add_u64 v[46:47], s[20:21], 0, v[2:3]
	v_or_b32_e32 v2, 0x1000, v0
	v_lshl_add_u64 v[50:51], s[20:21], 0, v[0:1]
	v_mbcnt_lo_u32_b32 v0, -1, 0
	v_or_b32_e32 v75, 4, v67
	v_or_b32_e32 v77, 8, v67
	v_or_b32_e32 v78, 12, v67
	v_or_b32_e32 v79, 16, v67
	v_or_b32_e32 v80, 20, v67
	v_or_b32_e32 v81, 24, v67
	v_or_b32_e32 v85, 28, v67
	v_or_b32_e32 v86, 64, v83
	v_or_b32_e32 v87, 0x4000, v63
	v_cmp_lt_u32_e64 s[0:1], 15, v83
	s_mul_i32 s39, s33, 0x9c4
	s_lshl_b32 s48, s33, 2
	v_or_b32_e32 v92, 0x200, v71
	v_or_b32_e32 v93, 0x204, v71
	v_or_b32_e32 v94, 0x100, v73
	v_lshl_add_u64 v[48:49], s[20:21], 0, v[2:3]
	s_mov_b32 s51, 0
	s_mov_b64 s[36:37], 0
	s_movk_i32 s49, 0x81
	s_mov_b32 s50, 0xff800000
	s_mov_b32 s38, 0x38d1b717
	v_mov_b32_e32 v95, 0xff800000
	v_mbcnt_hi_u32_b32 v96, -1, v0
	v_mov_b32_e32 v136, 0
	v_mov_b32_e32 v137, 0
	v_mov_b32_e32 v138, 0
	v_mov_b32_e32 v139, 0
	v_mov_b32_e32 v140, 0
	v_mov_b32_e32 v141, 0
	v_mov_b32_e32 v142, 0
	v_mov_b32_e32 v143, 0
	v_mov_b32_e32 v144, 0
	v_mov_b32_e32 v145, 0
	v_mov_b32_e32 v146, 0
	v_mov_b32_e32 v147, 0
	v_mov_b32_e32 v148, 0
	v_mov_b32_e32 v149, 0
	v_mov_b32_e32 v150, 0
	v_mov_b32_e32 v151, 0
	v_mov_b32_e32 v152, 0
	v_mov_b32_e32 v153, 0
	v_mov_b32_e32 v154, 0
	v_mov_b32_e32 v155, 0
	v_mov_b32_e32 v156, 0
	v_mov_b32_e32 v157, 0
	v_mov_b32_e32 v158, 0
	v_mov_b32_e32 v159, 0
	v_mov_b32_e32 v160, 0
	v_mov_b32_e32 v161, 0
	v_mov_b32_e32 v162, 0
	v_mov_b32_e32 v163, 0
	v_mov_b32_e32 v164, 0
	v_mov_b32_e32 v165, 0
	v_mov_b32_e32 v166, 0
	v_mov_b32_e32 v167, 0
	v_mov_b32_e32 v168, 0
	v_mov_b32_e32 v169, 0
	v_mov_b32_e32 v170, 0
	v_mov_b32_e32 v171, 0
	v_mov_b32_e32 v172, 0
	v_mov_b32_e32 v173, 0
	v_mov_b32_e32 v174, 0
	v_mov_b32_e32 v175, 0
	v_mov_b32_e32 v176, 0
	v_mov_b32_e32 v177, 0
	v_mov_b32_e32 v178, 0
	v_mov_b32_e32 v179, 0
	v_mov_b32_e32 v180, 0
	v_mov_b32_e32 v181, 0
	v_mov_b32_e32 v182, 0
	v_mov_b32_e32 v183, 0
	v_mov_b32_e32 v184, 0
	v_mov_b32_e32 v185, 0
	v_mov_b32_e32 v186, 0
	v_mov_b32_e32 v187, 0
	v_mov_b32_e32 v188, 0
	v_mov_b32_e32 v189, 0
	v_mov_b32_e32 v190, 0
	v_mov_b32_e32 v191, 0
	v_mov_b32_e32 v192, 0
	v_mov_b32_e32 v193, 0
	v_mov_b32_e32 v194, 0
	v_mov_b32_e32 v195, 0
	v_mov_b32_e32 v196, 0
	v_mov_b32_e32 v197, 0
	v_mov_b32_e32 v198, 0
	v_mov_b32_e32 v199, 0
	v_readfirstlane_b32 s54, v63
	s_lshr_b32 s54, s54, 12
	s_lshr_b32 s3, s54, 1
	s_and_b32 s54, s54, 1
	s_lshl_b32 s4, s2, 1
	s_add_u32 s4, s4, s3
	s_mul_i32 s5, s54, 0x1f4
	s_add_u32 s4, s4, s5
	v_mov_b32_e32 v82, s4
	s_lshl_b32 s5, s3, 13
	s_add_u32 s5, s5, 0x4000
	v_mov_b32_e32 v87, s5
	s_lshl_b32 s5, s3, 11
	s_add_u32 s5, s5, 0x8000
	v_mov_b32_e32 v88, s5
	s_lshl_b32 s5, s3, 4
	s_add_u32 s5, s5, 0x9008
	v_mov_b32_e32 v65, s5
	s_movk_i32 s3, 0x9c4
	v_mad_u32_u24 v90, v82, s3, v83
	v_lshlrev_b32_e32 v91, 2, v82
	s_branch .LBB1_9

.LBB1_9:
	s_mov_b32 s46, s54
	v_lshl_add_u32 v6, s46, 2, v65
	ds_read_b32 v0, v6
	s_waitcnt lgkmcnt(0)
	v_cmp_eq_u32_e32 vcc, 0, v0
	s_and_saveexec_b64 s[2:3], vcc
	s_cbranch_execz .LBB1_13
	s_mov_b64 s[4:5], 0

.LBB1_13:
	s_or_b64 exec, exec, s[2:3]
	s_mul_i32 s2, s51, s33
	v_add_u32_e32 v97, s2, v82
	v_readfirstlane_b32 s5, v0
	s_sub_i32 s5, s5, 1
	v_add_u32_e32 v7, -8, v6
	s_mov_b32 s16, 0x40000
.Lg_pollA:
	ds_read_b32 v1, v7
	s_waitcnt lgkmcnt(0)
	v_readfirstlane_b32 s4, v1
	s_cmp_lg_u32 s4, 0
	s_cbranch_scc1 .Lg_gotA
	s_sub_u32 s16, s16, 1
	s_cmp_eq_u32 s16, 0
	s_cbranch_scc1 .Lg_gotA
	s_sleep 1
	s_branch .Lg_pollA
.Lg_gotA:
	s_sub_i32 s4, s4, 1
	s_cmp_gt_u32 s4, 64
	s_cbranch_scc1 .Lg_fb
	s_cmp_gt_u32 s5, 64
	s_cbranch_scc1 .Lg_fb
	s_add_i32 s17, s4, s5
	s_cmp_gt_u32 s17, 64
	s_cbranch_scc1 .Lg_fb
	s_lshl_b32 s18, s46, 11
	v_cmp_gt_u32_e64 s[8:9], s4, v83
	v_subrev_u32_e32 v2, s4, v83
	v_add_u32_e32 v2, 0x100, v2
	v_cndmask_b32_e64 v2, v2, v83, s[8:9]
	v_lshl_add_u32 v1, v2, 4, v87
	v_add_u32_e32 v1, s18, v1
	s_lshl_b32 s18, s46, 9
	v_lshl_add_u32 v2, v2, 2, v88
	v_add_u32_e32 v2, s18, v2
	ds_read_b128 v[8:11], v1
	ds_read_b32 v12, v2
	v_cmp_gt_u32_e64 s[6:7], s17, v83
	v_lshlrev_b32_e32 v25, 4, v69
	s_waitcnt lgkmcnt(0)
	v_cmp_neq_f32_e32 vcc, 0, v8
	s_and_b64 s[8:9], vcc, s[6:7]
	v_cmp_neq_f32_e32 vcc, 0, v9
	s_and_b64 s[10:11], vcc, s[6:7]
	v_cmp_neq_f32_e32 vcc, 0, v10
	s_and_b64 s[12:13], vcc, s[6:7]
	v_cmp_neq_f32_e32 vcc, 0, v11
	s_and_b64 s[14:15], vcc, s[6:7]
	s_bcnt1_i32_b64 s16, s[8:9]
	s_bcnt1_i32_b64 s17, s[10:11]
	s_bcnt1_i32_b64 s18, s[12:13]
	s_bcnt1_i32_b64 s19, s[14:15]
	s_add_i32 s17, s17, s16
	s_add_i32 s18, s18, s17
	s_add_i32 s19, s19, s18
	s_cmp_eq_u32 s19, 0
	s_cbranch_scc1 .Lg_fb
	s_cmp_gt_u32 s19, 64
	s_cbranch_scc1 .Lg_fb
	v_mbcnt_lo_u32_b32 v13, s8, 0
	v_mbcnt_hi_u32_b32 v13, s9, v13
	v_lshl_add_u32 v14, v13, 3, v63
	v_mov_b32_e32 v4, v12
	v_mov_b32_e32 v5, v8
	s_mov_b64 exec, s[8:9]
	ds_write_b64 v14, v[4:5]
	s_mov_b64 exec, -1
	v_mbcnt_lo_u32_b32 v13, s10, 0
	v_mbcnt_hi_u32_b32 v13, s11, v13
	v_add_u32_e32 v13, s16, v13
	v_lshl_add_u32 v14, v13, 3, v63
	v_add_u32_e32 v4, 1, v12
	v_mov_b32_e32 v5, v9
	s_mov_b64 exec, s[10:11]
	ds_write_b64 v14, v[4:5]
	s_mov_b64 exec, -1
	v_mbcnt_lo_u32_b32 v13, s12, 0
	v_mbcnt_hi_u32_b32 v13, s13, v13
	v_add_u32_e32 v13, s17, v13
	v_lshl_add_u32 v14, v13, 3, v63
	v_add_u32_e32 v4, 2, v12
	v_mov_b32_e32 v5, v10
	s_mov_b64 exec, s[12:13]
	ds_write_b64 v14, v[4:5]
	s_mov_b64 exec, -1
	v_mbcnt_lo_u32_b32 v13, s14, 0
	v_mbcnt_hi_u32_b32 v13, s15, v13
	v_add_u32_e32 v13, s18, v13
	v_lshl_add_u32 v14, v13, 3, v63
	v_add_u32_e32 v4, 3, v12
	v_mov_b32_e32 v5, v11
	s_mov_b64 exec, s[14:15]
	ds_write_b64 v14, v[4:5]
	s_mov_b64 exec, -1
	v_mov_b32_e32 v4, 0
	ds_write_b32 v6, v4
	ds_write_b32 v7, v4
	v_cmp_gt_u32_e64 s[6:7], s19, v83
	v_lshl_add_u32 v14, v83, 3, v63
	ds_read_b64 v[16:17], v14
	v_lshl_add_u32 v22, v67, 3, v63
	ds_read_b32 v116, v22
	ds_read_b32 v117, v22 offset:32
	ds_read_b32 v118, v22 offset:64
	ds_read_b32 v119, v22 offset:96
	ds_read_b32 v120, v22 offset:128
	ds_read_b32 v121, v22 offset:160
	ds_read_b32 v122, v22 offset:192
	ds_read_b32 v123, v22 offset:224
	v_sub_u32_e32 v23, s19, v67
	s_waitcnt lgkmcnt(8)
	v_cndmask_b32_e64 v15, 0, v16, s[6:7]
	v_lshlrev_b32_e32 v15, 2, v15
	global_load_dword v18, v15, s[24:25]
	s_cmp_gt_u32 s19, 32
	s_cbranch_scc1 .Lg_big
	s_waitcnt lgkmcnt(0)
	v_cmp_lt_i32_e32 vcc, 0, v23
	v_lshl_add_u32 v24, v116, 8, v25
	s_mov_b64 exec, vcc
	global_load_dwordx4 v[136:139], v24, s[22:23]
	s_mov_b64 exec, -1
	v_cmp_lt_i32_e32 vcc, 4, v23
	v_lshl_add_u32 v24, v117, 8, v25
	s_mov_b64 exec, vcc
	global_load_dwordx4 v[140:143], v24, s[22:23]
	s_mov_b64 exec, -1
	v_cmp_lt_i32_e32 vcc, 8, v23
	v_lshl_add_u32 v24, v118, 8, v25
	s_mov_b64 exec, vcc
	global_load_dwordx4 v[144:147], v24, s[22:23]
	s_mov_b64 exec, -1
	v_cmp_lt_i32_e32 vcc, 12, v23
	v_lshl_add_u32 v24, v119, 8, v25
	s_mov_b64 exec, vcc
	global_load_dwordx4 v[148:151], v24, s[22:23]
	s_mov_b64 exec, -1
	v_cmp_lt_i32_e32 vcc, 16, v23
	v_lshl_add_u32 v24, v120, 8, v25
	s_mov_b64 exec, vcc
	global_load_dwordx4 v[152:155], v24, s[22:23]
	s_mov_b64 exec, -1
	v_cmp_lt_i32_e32 vcc, 20, v23
	v_lshl_add_u32 v24, v121, 8, v25
	s_mov_b64 exec, vcc
	global_load_dwordx4 v[156:159], v24, s[22:23]
	s_mov_b64 exec, -1
	v_cmp_lt_i32_e32 vcc, 24, v23
	v_lshl_add_u32 v24, v122, 8, v25
	s_mov_b64 exec, vcc
	global_load_dwordx4 v[160:163], v24, s[22:23]
	s_mov_b64 exec, -1
	v_cmp_lt_i32_e32 vcc, 28, v23
	v_lshl_add_u32 v24, v123, 8, v25
	s_mov_b64 exec, vcc
	global_load_dwordx4 v[164:167], v24, s[22:23]
	s_mov_b64 exec, -1
	s_waitcnt vmcnt(8)
	s_branch .Lg_soft

.Lg_fb:
	v_mov_b32_e32 v4, 0
	ds_write_b32 v7, v4
	v_mov_b32_e32 v0, 0xc8

.LBB1_217:
	s_andn2_saveexec_b64 s[0:1], s[30:31]
	s_cbranch_execz .LBB1_384
	v_readfirstlane_b32 s34, v1
	v_readfirstlane_b32 s36, v84
	v_and_b32_e32 v3, 63, v0
	v_lshlrev_b32_e32 v2, 4, v3
	s_cmp_lt_i32 s36, 0
	s_cbranch_scc1 .LBB1_384
	s_add_i32 s36, s36, 1
	s_lshl_b32 s36, s36, 1
	s_sub_i32 s36, s36, 1
	s_lshr_b32 s33, s33, 1
	s_and_b32 s55, s34, 1
	s_lshr_b32 s41, s34, 1
	s_mul_i32 s43, s55, 0x5000
	s_lshl_b32 s37, s2, 1
	s_add_u32 s37, s37, s41
	s_waitcnt lgkmcnt(0)
	s_and_b32 s29, s29, 0xffff
	s_mov_b32 s30, 0x17d78400
	s_mov_b32 s31, 0x20000
	s_mov_b32 s35, 0
	s_movk_i32 s7, 0x80
	s_mov_b32 s9, 0x7fffffff
	s_lshl_b32 s44, s34, 12
	s_add_u32 s44, s44, 0x4000
	s_lshl_b32 s45, s34, 10
	s_add_u32 s45, s45, 0x8000
	s_lshl_b32 s46, s34, 3
	s_add_u32 s46, s46, 0x9000
	s_mov_b32 s54, 0
	s_and_b32 s47, s37, 1
	s_lshl_b32 s47, s47, 2
	s_mul_i32 s38, s37, 0x9c40
	s_lshl_b32 s40, s47, 4
	s_sub_u32 s38, s38, s40
	s_add_u32 s38, s38, s43
.Lsc_row:
	v_subrev_u32_e32 v8, s47, v3
	v_lshlrev_b32_e32 v8, 2, v8
	s_mul_i32 s40, s55, 0x1400
	v_add_u32_e32 v8, s40, v8
	s_mov_b64 s[48:49], -1
	s_mov_b64 s[50:51], -1
	v_mov_b32_e32 v4, v2
	s_cmp_eq_u32 s55, 0
	s_cbranch_scc0 .Lsc_h1
	s_lshl_b64 s[48:49], -1, s47
	s_branch .Lsc_hd
.Lsc_h1:
	s_add_i32 s41, s47, 3
	v_min_u32_e32 v4, s41, v3
	v_lshlrev_b32_e32 v4, 4, v4
	s_lshl_b64 s[50:51], 2, s41
	s_sub_u32 s50, s50, 1
	s_subb_u32 s51, s51, 0
.Lsc_hd:
	s_and_b32 s41, s35, 1
	s_lshl_b32 s40, s41, 11
	s_add_u32 s40, s40, s44
	v_mov_b32_e32 v9, s40
	s_lshl_b32 s40, s41, 9
	s_add_u32 s40, s40, s45
	v_mov_b32_e32 v10, s40
	s_lshl_b32 s40, s41, 2
	s_add_u32 s40, s40, s46
	v_mov_b32_e32 v11, s40
	s_lshl_b32 s40, s41, 3
	s_add_u32 s40, s40, s54
	v_mov_b32_e32 v1, s40
	s_cmp_lt_i32 s35, s36
	s_cbranch_scc0 .Lsc_nonext
	s_add_i32 s52, s37, s33
	s_and_b32 s53, s52, 1
	s_lshl_b32 s53, s53, 2
	s_mul_i32 s39, s52, 0x9c40
	s_lshl_b32 s40, s53, 4
	s_sub_u32 s39, s39, s40
	s_add_u32 s39, s39, s43
	v_mov_b32_e32 v6, v2
	v_mov_b32_e32 v5, v2
	v_mov_b32_e32 v7, v2
	s_cmp_eq_u32 s55, 0
	s_cbranch_scc0 .Lsc_nh1
	v_max_u32_e32 v5, s53, v3
	v_lshlrev_b32_e32 v5, 4, v5
	s_branch .Lsc_gotnext
.Lsc_nh1:
	s_add_i32 s40, s53, 3
	v_min_u32_e32 v7, s40, v3
	v_lshlrev_b32_e32 v7, 4, v7
	s_branch .Lsc_gotnext

.Lsc_gotnext:
.Lsc_wait:
	ds_read_b32 v12, v11
	s_waitcnt lgkmcnt(0)
	v_readfirstlane_b32 s42, v12
	s_cmp_eq_u32 s42, 0
	s_cbranch_scc1 .Lsc_go
	s_sleep 2
	s_branch .Lsc_wait
.Lsc_go:
	s_mov_b32 s42, 0
	s_waitcnt vmcnt(9)
	v_or3_b32 v12, v100, v101, v102
	v_bitop3_b32 v12, v12, s9, v103 bitop3:0xc8
	v_cmp_ne_u32_e32 vcc, 0, v12
	s_and_b64 vcc, vcc, s[48:49]
	s_cbranch_vccz .Lsc_s0
	s_bcnt1_i32_b64 s40, vcc
	v_mbcnt_lo_u32_b32 v13, vcc_lo, 0
	v_mbcnt_hi_u32_b32 v13, vcc_hi, v13
	v_add_u32_e32 v13, s42, v13
	s_add_i32 s42, s42, s40
	v_cmp_gt_i32_e64 s[0:1], s7, v13
	s_and_b64 s[4:5], vcc, s[0:1]
	s_and_saveexec_b64 s[0:1], s[4:5]
	v_lshl_add_u32 v14, v13, 4, v9
	v_lshl_add_u32 v15, v13, 2, v10
	v_mov_b32_e32 v13, v8
	ds_write_b128 v14, v[100:103]
	ds_write_b32 v15, v13
	s_mov_b64 exec, -1
.Lsc_s0:
	s_add_u32 s40, s38, 0x2800
	buffer_load_dwordx4 v[100:103], v2, s[28:31], s40 offen nt
	s_waitcnt vmcnt(9)
	v_or3_b32 v12, v104, v105, v106
	v_bitop3_b32 v12, v12, s9, v107 bitop3:0xc8
	v_cmp_ne_u32_e32 vcc, 0, v12
	s_cbranch_vccz .Lsc_s1
	s_bcnt1_i32_b64 s40, vcc
	v_mbcnt_lo_u32_b32 v13, vcc_lo, 0
	v_mbcnt_hi_u32_b32 v13, vcc_hi, v13
	v_add_u32_e32 v13, s42, v13
	s_add_i32 s42, s42, s40
	v_cmp_gt_i32_e64 s[0:1], s7, v13
	s_and_b64 s[4:5], vcc, s[0:1]
	s_and_saveexec_b64 s[0:1], s[4:5]
	v_lshl_add_u32 v14, v13, 4, v9
	v_lshl_add_u32 v15, v13, 2, v10
	v_add_u32_e32 v13, 0x100, v8
	ds_write_b128 v14, v[104:107]
	ds_write_b32 v15, v13
	s_mov_b64 exec, -1
.Lsc_s1:
	s_add_u32 s40, s38, 0x2c00
	buffer_load_dwordx4 v[104:107], v2, s[28:31], s40 offen nt
	s_waitcnt vmcnt(9)
	v_or3_b32 v12, v108, v109, v110
	v_bitop3_b32 v12, v12, s9, v111 bitop3:0xc8
	v_cmp_ne_u32_e32 vcc, 0, v12
	s_cbranch_vccz .Lsc_s2
	s_bcnt1_i32_b64 s40, vcc
	v_mbcnt_lo_u32_b32 v13, vcc_lo, 0
	v_mbcnt_hi_u32_b32 v13, vcc_hi, v13
	v_add_u32_e32 v13, s42, v13
	s_add_i32 s42, s42, s40
	v_cmp_gt_i32_e64 s[0:1], s7, v13
	s_and_b64 s[4:5], vcc, s[0:1]
	s_and_saveexec_b64 s[0:1], s[4:5]
	v_lshl_add_u32 v14, v13, 4, v9
	v_lshl_add_u32 v15, v13, 2, v10
	v_add_u32_e32 v13, 0x200, v8
	ds_write_b128 v14, v[108:111]
	ds_write_b32 v15, v13
	s_mov_b64 exec, -1
.Lsc_s2:
	s_add_u32 s40, s38, 0x3000
	buffer_load_dwordx4 v[108:111], v2, s[28:31], s40 offen nt
	s_waitcnt vmcnt(9)
	v_or3_b32 v12, v112, v113, v114
	v_bitop3_b32 v12, v12, s9, v115 bitop3:0xc8
	v_cmp_ne_u32_e32 vcc, 0, v12
	s_cbranch_vccz .Lsc_s3
	s_bcnt1_i32_b64 s40, vcc
	v_mbcnt_lo_u32_b32 v13, vcc_lo, 0
	v_mbcnt_hi_u32_b32 v13, vcc_hi, v13
	v_add_u32_e32 v13, s42, v13
	s_add_i32 s42, s42, s40
	v_cmp_gt_i32_e64 s[0:1], s7, v13
	s_and_b64 s[4:5], vcc, s[0:1]
	s_and_saveexec_b64 s[0:1], s[4:5]
	v_lshl_add_u32 v14, v13, 4, v9
	v_lshl_add_u32 v15, v13, 2, v10
	v_add_u32_e32 v13, 0x300, v8
	ds_write_b128 v14, v[112:115]
	ds_write_b32 v15, v13
	s_mov_b64 exec, -1
.Lsc_s3:
	s_add_u32 s40, s38, 0x3400
	buffer_load_dwordx4 v[112:115], v2, s[28:31], s40 offen nt
	s_waitcnt vmcnt(9)
	v_or3_b32 v12, v116, v117, v118
	v_bitop3_b32 v12, v12, s9, v119 bitop3:0xc8
	v_cmp_ne_u32_e32 vcc, 0, v12
	s_cbranch_vccz .Lsc_s4
	s_bcnt1_i32_b64 s40, vcc
	v_mbcnt_lo_u32_b32 v13, vcc_lo, 0
	v_mbcnt_hi_u32_b32 v13, vcc_hi, v13
	v_add_u32_e32 v13, s42, v13
	s_add_i32 s42, s42, s40
	v_cmp_gt_i32_e64 s[0:1], s7, v13
	s_and_b64 s[4:5], vcc, s[0:1]
	s_and_saveexec_b64 s[0:1], s[4:5]
	v_lshl_add_u32 v14, v13, 4, v9
	v_lshl_add_u32 v15, v13, 2, v10
	v_add_u32_e32 v13, 0x400, v8
	ds_write_b128 v14, v[116:119]
	ds_write_b32 v15, v13
	s_mov_b64 exec, -1
.Lsc_s4:
	s_add_u32 s40, s38, 0x3800
	buffer_load_dwordx4 v[116:119], v2, s[28:31], s40 offen nt
	s_waitcnt vmcnt(9)
	v_or3_b32 v12, v120, v121, v122
	v_bitop3_b32 v12, v12, s9, v123 bitop3:0xc8
	v_cmp_ne_u32_e32 vcc, 0, v12
	s_cbranch_vccz .Lsc_s5
	s_bcnt1_i32_b64 s40, vcc
	v_mbcnt_lo_u32_b32 v13, vcc_lo, 0
	v_mbcnt_hi_u32_b32 v13, vcc_hi, v13
	v_add_u32_e32 v13, s42, v13
	s_add_i32 s42, s42, s40
	v_cmp_gt_i32_e64 s[0:1], s7, v13
	s_and_b64 s[4:5], vcc, s[0:1]
	s_and_saveexec_b64 s[0:1], s[4:5]
	v_lshl_add_u32 v14, v13, 4, v9
	v_lshl_add_u32 v15, v13, 2, v10
	v_add_u32_e32 v13, 0x500, v8
	ds_write_b128 v14, v[120:123]
	ds_write_b32 v15, v13
	s_mov_b64 exec, -1
.Lsc_s5:
	s_add_u32 s40, s38, 0x3c00
	buffer_load_dwordx4 v[120:123], v2, s[28:31], s40 offen nt
	s_waitcnt vmcnt(9)
	v_or3_b32 v12, v124, v125, v126
	v_bitop3_b32 v12, v12, s9, v127 bitop3:0xc8
	v_cmp_ne_u32_e32 vcc, 0, v12
	s_cbranch_vccz .Lsc_s6
	s_bcnt1_i32_b64 s40, vcc
	v_mbcnt_lo_u32_b32 v13, vcc_lo, 0
	v_mbcnt_hi_u32_b32 v13, vcc_hi, v13
	v_add_u32_e32 v13, s42, v13
	s_add_i32 s42, s42, s40
	v_cmp_gt_i32_e64 s[0:1], s7, v13
	s_and_b64 s[4:5], vcc, s[0:1]
	s_and_saveexec_b64 s[0:1], s[4:5]
	v_lshl_add_u32 v14, v13, 4, v9
	v_lshl_add_u32 v15, v13, 2, v10
	v_add_u32_e32 v13, 0x600, v8
	ds_write_b128 v14, v[124:127]
	ds_write_b32 v15, v13
	s_mov_b64 exec, -1
.Lsc_s6:
	s_add_u32 s40, s38, 0x4000
	buffer_load_dwordx4 v[124:127], v2, s[28:31], s40 offen nt
	s_waitcnt vmcnt(9)
	v_or3_b32 v12, v128, v129, v130
	v_bitop3_b32 v12, v12, s9, v131 bitop3:0xc8
	v_cmp_ne_u32_e32 vcc, 0, v12
	s_cbranch_vccz .Lsc_s7
	s_bcnt1_i32_b64 s40, vcc
	v_mbcnt_lo_u32_b32 v13, vcc_lo, 0
	v_mbcnt_hi_u32_b32 v13, vcc_hi, v13
	v_add_u32_e32 v13, s42, v13
	s_add_i32 s42, s42, s40
	v_cmp_gt_i32_e64 s[0:1], s7, v13
	s_and_b64 s[4:5], vcc, s[0:1]
	s_and_saveexec_b64 s[0:1], s[4:5]
	v_lshl_add_u32 v14, v13, 4, v9
	v_lshl_add_u32 v15, v13, 2, v10
	v_add_u32_e32 v13, 0x700, v8
	ds_write_b128 v14, v[128:131]
	ds_write_b32 v15, v13
	s_mov_b64 exec, -1
.Lsc_s7:
	s_add_u32 s40, s38, 0x4400
	buffer_load_dwordx4 v[128:131], v2, s[28:31], s40 offen nt
	s_waitcnt vmcnt(9)
	v_or3_b32 v12, v132, v133, v134
	v_bitop3_b32 v12, v12, s9, v135 bitop3:0xc8
	v_cmp_ne_u32_e32 vcc, 0, v12
	s_cbranch_vccz .Lsc_s8
	s_bcnt1_i32_b64 s40, vcc
	v_mbcnt_lo_u32_b32 v13, vcc_lo, 0
	v_mbcnt_hi_u32_b32 v13, vcc_hi, v13
	v_add_u32_e32 v13, s42, v13
	s_add_i32 s42, s42, s40
	v_cmp_gt_i32_e64 s[0:1], s7, v13
	s_and_b64 s[4:5], vcc, s[0:1]
	s_and_saveexec_b64 s[0:1], s[4:5]
	v_lshl_add_u32 v14, v13, 4, v9
	v_lshl_add_u32 v15, v13, 2, v10
	v_add_u32_e32 v13, 0x800, v8
	ds_write_b128 v14, v[132:135]
	ds_write_b32 v15, v13
	s_mov_b64 exec, -1
.Lsc_s8:
	s_add_u32 s40, s38, 0x4800
	buffer_load_dwordx4 v[132:135], v2, s[28:31], s40 offen nt
	s_waitcnt vmcnt(9)
	v_or3_b32 v12, v136, v137, v138
	v_bitop3_b32 v12, v12, s9, v139 bitop3:0xc8
	v_cmp_ne_u32_e32 vcc, 0, v12
	s_cbranch_vccz .Lsc_s9
	s_bcnt1_i32_b64 s40, vcc
	v_mbcnt_lo_u32_b32 v13, vcc_lo, 0
	v_mbcnt_hi_u32_b32 v13, vcc_hi, v13
	v_add_u32_e32 v13, s42, v13
	s_add_i32 s42, s42, s40
	v_cmp_gt_i32_e64 s[0:1], s7, v13
	s_and_b64 s[4:5], vcc, s[0:1]
	s_and_saveexec_b64 s[0:1], s[4:5]
	v_lshl_add_u32 v14, v13, 4, v9
	v_lshl_add_u32 v15, v13, 2, v10
	v_add_u32_e32 v13, 0x900, v8
	ds_write_b128 v14, v[136:139]
	ds_write_b32 v15, v13
	s_mov_b64 exec, -1
.Lsc_s9:
	s_add_u32 s40, s38, 0x4c00
	buffer_load_dwordx4 v[136:139], v4, s[28:31], s40 offen nt
	s_waitcnt vmcnt(9)
	v_or3_b32 v12, v100, v101, v102
	v_bitop3_b32 v12, v12, s9, v103 bitop3:0xc8
	v_cmp_ne_u32_e32 vcc, 0, v12
	s_cbranch_vccz .Lsc_s10
	s_bcnt1_i32_b64 s40, vcc
	v_mbcnt_lo_u32_b32 v13, vcc_lo, 0
	v_mbcnt_hi_u32_b32 v13, vcc_hi, v13
	v_add_u32_e32 v13, s42, v13
	s_add_i32 s42, s42, s40
	v_cmp_gt_i32_e64 s[0:1], s7, v13
	s_and_b64 s[4:5], vcc, s[0:1]
	s_and_saveexec_b64 s[0:1], s[4:5]
	v_lshl_add_u32 v14, v13, 4, v9
	v_lshl_add_u32 v15, v13, 2, v10
	v_add_u32_e32 v13, 0xa00, v8
	ds_write_b128 v14, v[100:103]
	ds_write_b32 v15, v13
	s_mov_b64 exec, -1
.Lsc_s10:
	s_mov_b32 s40, s39
	buffer_load_dwordx4 v[100:103], v5, s[28:31], s40 offen nt
	s_waitcnt vmcnt(9)
	v_or3_b32 v12, v104, v105, v106
	v_bitop3_b32 v12, v12, s9, v107 bitop3:0xc8
	v_cmp_ne_u32_e32 vcc, 0, v12
	s_cbranch_vccz .Lsc_s11
	s_bcnt1_i32_b64 s40, vcc
	v_mbcnt_lo_u32_b32 v13, vcc_lo, 0
	v_mbcnt_hi_u32_b32 v13, vcc_hi, v13
	v_add_u32_e32 v13, s42, v13
	s_add_i32 s42, s42, s40
	v_cmp_gt_i32_e64 s[0:1], s7, v13
	s_and_b64 s[4:5], vcc, s[0:1]
	s_and_saveexec_b64 s[0:1], s[4:5]
	v_lshl_add_u32 v14, v13, 4, v9
	v_lshl_add_u32 v15, v13, 2, v10
	v_add_u32_e32 v13, 0xb00, v8
	ds_write_b128 v14, v[104:107]
	ds_write_b32 v15, v13
	s_mov_b64 exec, -1
.Lsc_s11:
	s_add_u32 s40, s39, 0x400
	buffer_load_dwordx4 v[104:107], v6, s[28:31], s40 offen nt
	s_waitcnt vmcnt(9)
	v_or3_b32 v12, v108, v109, v110
	v_bitop3_b32 v12, v12, s9, v111 bitop3:0xc8
	v_cmp_ne_u32_e32 vcc, 0, v12
	s_cbranch_vccz .Lsc_s12
	s_bcnt1_i32_b64 s40, vcc
	v_mbcnt_lo_u32_b32 v13, vcc_lo, 0
	v_mbcnt_hi_u32_b32 v13, vcc_hi, v13
	v_add_u32_e32 v13, s42, v13
	s_add_i32 s42, s42, s40
	v_cmp_gt_i32_e64 s[0:1], s7, v13
	s_and_b64 s[4:5], vcc, s[0:1]
	s_and_saveexec_b64 s[0:1], s[4:5]
	v_lshl_add_u32 v14, v13, 4, v9
	v_lshl_add_u32 v15, v13, 2, v10
	v_add_u32_e32 v13, 0xc00, v8
	ds_write_b128 v14, v[108:111]
	ds_write_b32 v15, v13
	s_mov_b64 exec, -1
.Lsc_s12:
	s_add_u32 s40, s39, 0x800
	buffer_load_dwordx4 v[108:111], v6, s[28:31], s40 offen nt
	s_waitcnt vmcnt(9)
	v_or3_b32 v12, v112, v113, v114
	v_bitop3_b32 v12, v12, s9, v115 bitop3:0xc8
	v_cmp_ne_u32_e32 vcc, 0, v12
	s_cbranch_vccz .Lsc_s13
	s_bcnt1_i32_b64 s40, vcc
	v_mbcnt_lo_u32_b32 v13, vcc_lo, 0
	v_mbcnt_hi_u32_b32 v13, vcc_hi, v13
	v_add_u32_e32 v13, s42, v13
	s_add_i32 s42, s42, s40
	v_cmp_gt_i32_e64 s[0:1], s7, v13
	s_and_b64 s[4:5], vcc, s[0:1]
	s_and_saveexec_b64 s[0:1], s[4:5]
	v_lshl_add_u32 v14, v13, 4, v9
	v_lshl_add_u32 v15, v13, 2, v10
	v_add_u32_e32 v13, 0xd00, v8
	ds_write_b128 v14, v[112:115]
	ds_write_b32 v15, v13
	s_mov_b64 exec, -1
.Lsc_s13:
	s_add_u32 s40, s39, 0xc00
	buffer_load_dwordx4 v[112:115], v6, s[28:31], s40 offen nt
	s_waitcnt vmcnt(9)
	v_or3_b32 v12, v116, v117, v118
	v_bitop3_b32 v12, v12, s9, v119 bitop3:0xc8
	v_cmp_ne_u32_e32 vcc, 0, v12
	s_cbranch_vccz .Lsc_s14
	s_bcnt1_i32_b64 s40, vcc
	v_mbcnt_lo_u32_b32 v13, vcc_lo, 0
	v_mbcnt_hi_u32_b32 v13, vcc_hi, v13
	v_add_u32_e32 v13, s42, v13
	s_add_i32 s42, s42, s40
	v_cmp_gt_i32_e64 s[0:1], s7, v13
	s_and_b64 s[4:5], vcc, s[0:1]
	s_and_saveexec_b64 s[0:1], s[4:5]
	v_lshl_add_u32 v14, v13, 4, v9
	v_lshl_add_u32 v15, v13, 2, v10
	v_add_u32_e32 v13, 0xe00, v8
	ds_write_b128 v14, v[116:119]
	ds_write_b32 v15, v13
	s_mov_b64 exec, -1
.Lsc_s14:
	s_add_u32 s40, s39, 0x1000
	buffer_load_dwordx4 v[116:119], v6, s[28:31], s40 offen nt
	s_waitcnt vmcnt(9)
	v_or3_b32 v12, v120, v121, v122
	v_bitop3_b32 v12, v12, s9, v123 bitop3:0xc8
	v_cmp_ne_u32_e32 vcc, 0, v12
	s_cbranch_vccz .Lsc_s15
	s_bcnt1_i32_b64 s40, vcc
	v_mbcnt_lo_u32_b32 v13, vcc_lo, 0
	v_mbcnt_hi_u32_b32 v13, vcc_hi, v13
	v_add_u32_e32 v13, s42, v13
	s_add_i32 s42, s42, s40
	v_cmp_gt_i32_e64 s[0:1], s7, v13
	s_and_b64 s[4:5], vcc, s[0:1]
	s_and_saveexec_b64 s[0:1], s[4:5]
	v_lshl_add_u32 v14, v13, 4, v9
	v_lshl_add_u32 v15, v13, 2, v10
	v_add_u32_e32 v13, 0xf00, v8
	ds_write_b128 v14, v[120:123]
	ds_write_b32 v15, v13
	s_mov_b64 exec, -1
.Lsc_s15:
	s_add_u32 s40, s39, 0x1400
	buffer_load_dwordx4 v[120:123], v6, s[28:31], s40 offen nt
	s_waitcnt vmcnt(9)
	v_or3_b32 v12, v124, v125, v126
	v_bitop3_b32 v12, v12, s9, v127 bitop3:0xc8
	v_cmp_ne_u32_e32 vcc, 0, v12
	s_cbranch_vccz .Lsc_s16
	s_bcnt1_i32_b64 s40, vcc
	v_mbcnt_lo_u32_b32 v13, vcc_lo, 0
	v_mbcnt_hi_u32_b32 v13, vcc_hi, v13
	v_add_u32_e32 v13, s42, v13
	s_add_i32 s42, s42, s40
	v_cmp_gt_i32_e64 s[0:1], s7, v13
	s_and_b64 s[4:5], vcc, s[0:1]
	s_and_saveexec_b64 s[0:1], s[4:5]
	v_lshl_add_u32 v14, v13, 4, v9
	v_lshl_add_u32 v15, v13, 2, v10
	v_add_u32_e32 v13, 0x1000, v8
	ds_write_b128 v14, v[124:127]
	ds_write_b32 v15, v13
	s_mov_b64 exec, -1
.Lsc_s16:
	s_add_u32 s40, s39, 0x1800
	buffer_load_dwordx4 v[124:127], v6, s[28:31], s40 offen nt
	s_waitcnt vmcnt(9)
	v_or3_b32 v12, v128, v129, v130
	v_bitop3_b32 v12, v12, s9, v131 bitop3:0xc8
	v_cmp_ne_u32_e32 vcc, 0, v12
	s_cbranch_vccz .Lsc_s17
	s_bcnt1_i32_b64 s40, vcc
	v_mbcnt_lo_u32_b32 v13, vcc_lo, 0
	v_mbcnt_hi_u32_b32 v13, vcc_hi, v13
	v_add_u32_e32 v13, s42, v13
	s_add_i32 s42, s42, s40
	v_cmp_gt_i32_e64 s[0:1], s7, v13
	s_and_b64 s[4:5], vcc, s[0:1]
	s_and_saveexec_b64 s[0:1], s[4:5]
	v_lshl_add_u32 v14, v13, 4, v9
	v_lshl_add_u32 v15, v13, 2, v10
	v_add_u32_e32 v13, 0x1100, v8
	ds_write_b128 v14, v[128:131]
	ds_write_b32 v15, v13
	s_mov_b64 exec, -1
.Lsc_s17:
	s_add_u32 s40, s39, 0x1c00
	buffer_load_dwordx4 v[128:131], v6, s[28:31], s40 offen nt
	s_waitcnt vmcnt(9)
	v_or3_b32 v12, v132, v133, v134
	v_bitop3_b32 v12, v12, s9, v135 bitop3:0xc8
	v_cmp_ne_u32_e32 vcc, 0, v12
	s_cbranch_vccz .Lsc_s18
	s_bcnt1_i32_b64 s40, vcc
	v_mbcnt_lo_u32_b32 v13, vcc_lo, 0
	v_mbcnt_hi_u32_b32 v13, vcc_hi, v13
	v_add_u32_e32 v13, s42, v13
	s_add_i32 s42, s42, s40
	v_cmp_gt_i32_e64 s[0:1], s7, v13
	s_and_b64 s[4:5], vcc, s[0:1]
	s_and_saveexec_b64 s[0:1], s[4:5]
	v_lshl_add_u32 v14, v13, 4, v9
	v_lshl_add_u32 v15, v13, 2, v10
	v_add_u32_e32 v13, 0x1200, v8
	ds_write_b128 v14, v[132:135]
	ds_write_b32 v15, v13
	s_mov_b64 exec, -1
.Lsc_s18:
	s_add_u32 s40, s39, 0x2000
	buffer_load_dwordx4 v[132:135], v6, s[28:31], s40 offen nt
	s_waitcnt vmcnt(9)
	v_or3_b32 v12, v136, v137, v138
	v_bitop3_b32 v12, v12, s9, v139 bitop3:0xc8
	v_cmp_ne_u32_e32 vcc, 0, v12
	s_and_b64 vcc, vcc, s[50:51]
	s_cbranch_vccz .Lsc_s19
	s_bcnt1_i32_b64 s40, vcc
	v_mbcnt_lo_u32_b32 v13, vcc_lo, 0
	v_mbcnt_hi_u32_b32 v13, vcc_hi, v13
	v_add_u32_e32 v13, s42, v13
	s_add_i32 s42, s42, s40
	v_cmp_gt_i32_e64 s[0:1], s7, v13
	s_and_b64 s[4:5], vcc, s[0:1]
	s_and_saveexec_b64 s[0:1], s[4:5]
	v_lshl_add_u32 v14, v13, 4, v9
	v_lshl_add_u32 v15, v13, 2, v10
	v_add_u32_e32 v13, 0x1300, v8
	ds_write_b128 v14, v[136:139]
	ds_write_b32 v15, v13
	s_mov_b64 exec, -1

	.amdhsa_kernel _Z11attn_kernelPKfS0_PKDv8_DF16_S0_Pfi
		.amdhsa_group_segment_fixed_size 36896
		.amdhsa_private_segment_fixed_size 0
		.amdhsa_kernarg_size 44
		.amdhsa_user_sgpr_count 2
		.amdhsa_user_sgpr_dispatch_ptr 0
		.amdhsa_user_sgpr_queue_ptr 0
		.amdhsa_user_sgpr_kernarg_segment_ptr 1
		.amdhsa_user_sgpr_dispatch_id 0
		.amdhsa_user_sgpr_kernarg_preload_length 0
		.amdhsa_user_sgpr_kernarg_preload_offset 0
		.amdhsa_user_sgpr_private_segment_size 0
		.amdhsa_uses_dynamic_stack 0
		.amdhsa_enable_private_segment 0
		.amdhsa_system_sgpr_workgroup_id_x 1
		.amdhsa_system_sgpr_workgroup_id_y 0
		.amdhsa_system_sgpr_workgroup_id_z 0
		.amdhsa_system_sgpr_workgroup_info 0
		.amdhsa_system_vgpr_workitem_id 0
		.amdhsa_next_free_vgpr 248
		.amdhsa_next_free_sgpr 58
		.amdhsa_accum_offset 248
		.amdhsa_reserve_vcc 1
		.amdhsa_float_round_mode_32 0
		.amdhsa_float_round_mode_16_64 0
		.amdhsa_float_denorm_mode_32 3
		.amdhsa_float_denorm_mode_16_64 3
		.amdhsa_dx10_clamp 1
		.amdhsa_ieee_mode 1
		.amdhsa_fp16_overflow 0
		.amdhsa_tg_split 0
		.amdhsa_exception_fp_ieee_invalid_op 0
		.amdhsa_exception_fp_denorm_src 0
		.amdhsa_exception_fp_ieee_div_zero 0
		.amdhsa_exception_fp_ieee_overflow 0
		.amdhsa_exception_fp_ieee_underflow 0
		.amdhsa_exception_fp_ieee_inexact 0
		.amdhsa_exception_int_div_zero 0
	.end_amdhsa_kernel

.Lfunc_end1:
	.size	_Z11attn_kernelPKfS0_PKDv8_DF16_S0_Pfi, .Lfunc_end1-_Z11attn_kernelPKfS0_PKDv8_DF16_S0_Pfi
	.set _Z11attn_kernelPKfS0_PKDv8_DF16_S0_Pfi.num_vgpr, 248
	.set _Z11attn_kernelPKfS0_PKDv8_DF16_S0_Pfi.num_agpr, 0
	.set _Z11attn_kernelPKfS0_PKDv8_DF16_S0_Pfi.numbered_sgpr, 58
	.set _Z11attn_kernelPKfS0_PKDv8_DF16_S0_Pfi.num_named_barrier, 0
	.set _Z11attn_kernelPKfS0_PKDv8_DF16_S0_Pfi.private_seg_size, 0
	.set _Z11attn_kernelPKfS0_PKDv8_DF16_S0_Pfi.uses_vcc, 1
	.set _Z11attn_kernelPKfS0_PKDv8_DF16_S0_Pfi.uses_flat_scratch, 0
	.set _Z11attn_kernelPKfS0_PKDv8_DF16_S0_Pfi.has_dyn_sized_stack, 0
	.set _Z11attn_kernelPKfS0_PKDv8_DF16_S0_Pfi.has_recursion, 0
	.set _Z11attn_kernelPKfS0_PKDv8_DF16_S0_Pfi.has_indirect_call, 0

amdhsa.kernels:
  - .agpr_count:     0
    .args:
      - .actual_access:  read_only
        .address_space:  global
        .offset:         0
        .size:           8
        .value_kind:     global_buffer
      - .actual_access:  read_only
        .address_space:  global
        .offset:         8
        .size:           8
        .value_kind:     global_buffer
      - .actual_access:  write_only
        .address_space:  global
        .offset:         16
        .size:           8
        .value_kind:     global_buffer
      - .actual_access:  write_only
        .address_space:  global
        .offset:         24
        .size:           8
        .value_kind:     global_buffer
      - .offset:         32
        .size:           4
        .value_kind:     hidden_block_count_x
      - .offset:         36
        .size:           4
        .value_kind:     hidden_block_count_y
      - .offset:         40
        .size:           4
        .value_kind:     hidden_block_count_z
      - .offset:         44
        .size:           2
        .value_kind:     hidden_group_size_x
      - .offset:         46
        .size:           2
        .value_kind:     hidden_group_size_y
      - .offset:         48
        .size:           2
        .value_kind:     hidden_group_size_z
      - .offset:         50
        .size:           2
        .value_kind:     hidden_remainder_x
      - .offset:         52
        .size:           2
        .value_kind:     hidden_remainder_y
      - .offset:         54
        .size:           2
        .value_kind:     hidden_remainder_z
      - .offset:         72
        .size:           8
        .value_kind:     hidden_global_offset_x
      - .offset:         80
        .size:           8
        .value_kind:     hidden_global_offset_y
      - .offset:         88
        .size:           8
        .value_kind:     hidden_global_offset_z
      - .offset:         96
        .size:           2
        .value_kind:     hidden_grid_dims
    .group_segment_fixed_size: 0
    .kernarg_segment_align: 8
    .kernarg_segment_size: 288
    .language:       OpenCL C
    .language_version:
      - 2
      - 0
    .max_flat_workgroup_size: 256
    .name:           _Z11prep_kernelPKfS0_PfPDv4_DF16_
    .private_segment_fixed_size: 0
    .sgpr_count:     20
    .sgpr_spill_count: 0
    .symbol:         _Z11prep_kernelPKfS0_PfPDv4_DF16_.kd
    .uniform_work_group_size: 1
    .uses_dynamic_stack: false
    .vgpr_count:     17
    .vgpr_spill_count: 0
    .wavefront_size: 64
  - .agpr_count:     0
    .args:
      - .actual_access:  read_only
        .address_space:  global
        .offset:         0
        .size:           8
        .value_kind:     global_buffer
      - .actual_access:  read_only
        .address_space:  global
        .offset:         8
        .size:           8
        .value_kind:     global_buffer
      - .actual_access:  read_only
        .address_space:  global
        .offset:         16
        .size:           8
        .value_kind:     global_buffer
      - .actual_access:  read_only
        .address_space:  global
        .offset:         24
        .size:           8
        .value_kind:     global_buffer
      - .actual_access:  write_only
        .address_space:  global
        .offset:         32
        .size:           8
        .value_kind:     global_buffer
      - .offset:         40
        .size:           4
        .value_kind:     by_value
    .group_segment_fixed_size: 36896
    .kernarg_segment_align: 8
    .kernarg_segment_size: 44
    .language:       OpenCL C
    .language_version:
      - 2
      - 0
    .max_flat_workgroup_size: 512
    .name:           _Z11attn_kernelPKfS0_PKDv8_DF16_S0_Pfi
    .private_segment_fixed_size: 0
    .sgpr_count:     64
    .sgpr_spill_count: 0
    .symbol:         _Z11attn_kernelPKfS0_PKDv8_DF16_S0_Pfi.kd
    .uniform_work_group_size: 1
    .uses_dynamic_stack: false
    .vgpr_count:     248
    .vgpr_spill_count: 0
    .wavefront_size: 64
